# baseline (speedup 1.0000x reference)
_Z9k_gemm_tlILi3ELb0EEvPKDF16_6TlArgs:
	s_load_dwordx4 s[8:11], s[0:1], 0x0
	s_load_dwordx4 s[4:7], s[0:1], 0x30
	v_lshrrev_b32_e32 v43, 6, v0
	s_lshl_b32 s1, s2, 6
	v_lshl_or_b32 v34, s3, 2, v43
	v_mov_b32_e32 v35, 0
	s_lshr_b32 s0, s2, 6
	s_and_b32 s2, s1, 0xfc0
	s_mov_b32 s1, 0
	v_lshlrev_b64 v[2:3], 15, v[34:35]
	s_lshl_b32 s12, s3, 7
	v_lshrrev_b32_e32 v48, 4, v0
	v_or_b32_e32 v48, s12, v48
	v_lshlrev_b32_e32 v48, 2, v48
	v_lshlrev_b32_e32 v42, 4, v0
	v_lshrrev_b32_e32 v44, 3, v0
	v_or_b32_e32 v1, 0x100, v0
	v_lshrrev_b32_e32 v14, 3, v1
	s_waitcnt lgkmcnt(0)
	global_load_dword v240, v48, s[4:5]
	global_load_dword v242, v48, s[4:5] offset:64
	global_load_dword v244, v48, s[4:5] offset:128
	global_load_dword v246, v48, s[4:5] offset:192
	global_load_dword v248, v48, s[4:5] offset:256
	global_load_dword v250, v48, s[4:5] offset:320
	global_load_dword v252, v48, s[4:5] offset:384
	global_load_dword v254, v48, s[4:5] offset:448
	v_lshl_add_u64 v[2:3], s[8:9], 0, v[2:3]
	s_lshl_b64 s[8:9], s[0:1], 22
	s_add_u32 s8, s10, s8
	s_addc_u32 s9, s11, s9
	s_lshl_b32 s10, s2, 1
	v_and_b32_e32 v34, 0x3f0, v42
	s_add_u32 s8, s8, s10
	v_lshl_add_u64 v[36:37], v[2:3], 0, v[34:35]
	s_addc_u32 s9, s9, 0
	v_and_b32_e32 v34, 0x70, v42
	v_lshl_add_u64 v[2:3], s[8:9], 0, v[34:35]
	v_lshlrev_b32_e32 v4, 13, v44
	v_mov_b32_e32 v5, v35
	v_lshl_add_u64 v[38:39], v[2:3], 0, v[4:5]
	v_lshlrev_b32_e32 v4, 13, v14
	v_lshl_add_u64 v[40:41], v[2:3], 0, v[4:5]
	s_mov_b32 s14, 0x1000
	s_mov_b32 s15, 0
	s_mov_b32 s16, 0x80000
	s_mov_b32 s17, 0
	global_load_dwordx4 v[64:67], v[38:39], off
	global_load_dwordx4 v[68:71], v[40:41], off
	v_lshl_add_u64 v[38:39], v[38:39], 0, s[16:17]
	v_lshl_add_u64 v[40:41], v[40:41], 0, s[16:17]
	global_load_dwordx4 v[128:131], v[36:37], off
	global_load_dwordx4 v[132:135], v[36:37], off offset:1024
	global_load_dwordx4 v[136:139], v[36:37], off offset:2048
	global_load_dwordx4 v[140:143], v[36:37], off offset:3072
	v_lshl_add_u64 v[36:37], v[36:37], 0, s[14:15]
	global_load_dwordx4 v[72:75], v[38:39], off
	global_load_dwordx4 v[76:79], v[40:41], off
	v_lshl_add_u64 v[38:39], v[38:39], 0, s[16:17]
	v_lshl_add_u64 v[40:41], v[40:41], 0, s[16:17]
	global_load_dwordx4 v[144:147], v[36:37], off
	global_load_dwordx4 v[148:151], v[36:37], off offset:1024
	global_load_dwordx4 v[152:155], v[36:37], off offset:2048
	global_load_dwordx4 v[156:159], v[36:37], off offset:3072
	v_lshl_add_u64 v[36:37], v[36:37], 0, s[14:15]
	global_load_dwordx4 v[80:83], v[38:39], off
	global_load_dwordx4 v[84:87], v[40:41], off
	v_lshl_add_u64 v[38:39], v[38:39], 0, s[16:17]
	v_lshl_add_u64 v[40:41], v[40:41], 0, s[16:17]
	global_load_dwordx4 v[160:163], v[36:37], off
	global_load_dwordx4 v[164:167], v[36:37], off offset:1024
	global_load_dwordx4 v[168:171], v[36:37], off offset:2048
	global_load_dwordx4 v[172:175], v[36:37], off offset:3072
	v_lshl_add_u64 v[36:37], v[36:37], 0, s[14:15]
	global_load_dwordx4 v[88:91], v[38:39], off
	global_load_dwordx4 v[92:95], v[40:41], off
	v_lshl_add_u64 v[38:39], v[38:39], 0, s[16:17]
	v_lshl_add_u64 v[40:41], v[40:41], 0, s[16:17]
	global_load_dwordx4 v[176:179], v[36:37], off
	global_load_dwordx4 v[180:183], v[36:37], off offset:1024
	global_load_dwordx4 v[184:187], v[36:37], off offset:2048
	global_load_dwordx4 v[188:191], v[36:37], off offset:3072
	v_lshl_add_u64 v[36:37], v[36:37], 0, s[14:15]
	global_load_dwordx4 v[96:99], v[38:39], off
	global_load_dwordx4 v[100:103], v[40:41], off
	v_lshl_add_u64 v[38:39], v[38:39], 0, s[16:17]
	v_lshl_add_u64 v[40:41], v[40:41], 0, s[16:17]
	global_load_dwordx4 v[192:195], v[36:37], off
	global_load_dwordx4 v[196:199], v[36:37], off offset:1024
	global_load_dwordx4 v[200:203], v[36:37], off offset:2048
	global_load_dwordx4 v[204:207], v[36:37], off offset:3072
	v_lshl_add_u64 v[36:37], v[36:37], 0, s[14:15]
	global_load_dwordx4 v[104:107], v[38:39], off
	global_load_dwordx4 v[108:111], v[40:41], off
	v_lshl_add_u64 v[38:39], v[38:39], 0, s[16:17]
	v_lshl_add_u64 v[40:41], v[40:41], 0, s[16:17]
	global_load_dwordx4 v[208:211], v[36:37], off
	global_load_dwordx4 v[212:215], v[36:37], off offset:1024
	global_load_dwordx4 v[216:219], v[36:37], off offset:2048
	global_load_dwordx4 v[220:223], v[36:37], off offset:3072
	v_lshl_add_u64 v[36:37], v[36:37], 0, s[14:15]
	global_load_dwordx4 v[112:115], v[38:39], off
	global_load_dwordx4 v[116:119], v[40:41], off
	v_lshl_add_u64 v[38:39], v[38:39], 0, s[16:17]
	v_lshl_add_u64 v[40:41], v[40:41], 0, s[16:17]
	global_load_dwordx4 v[224:227], v[36:37], off
	global_load_dwordx4 v[228:231], v[36:37], off offset:1024
	global_load_dwordx4 v[232:235], v[36:37], off offset:2048
	global_load_dwordx4 v[236:239], v[36:37], off offset:3072
	v_lshl_add_u64 v[36:37], v[36:37], 0, s[14:15]
	global_load_dwordx4 v[120:123], v[38:39], off
	global_load_dwordx4 v[124:127], v[40:41], off
	v_lshrrev_b32_e32 v11, 2, v0
	v_lshlrev_b32_e32 v10, 3, v0
	v_and_b32_e32 v12, 16, v0
	v_and_b32_e32 v11, 11, v11
	v_and_b32_e32 v10, 24, v10
	v_lshlrev_b32_e32 v12, 1, v12
	v_mul_u32_u24_e32 v11, 0x90, v11
	v_add3_u32 v45, v11, v10, v12
	s_movk_i32 s11, 0x90
	v_mad_u32_u24 v46, v44, s11, v34
	v_mad_u32_u24 v47, v14, s11, v34
	s_lshl_b32 s3, s3, 7
	s_lshl_b64 s[0:1], s[0:1], 23
	s_add_u32 s0, s6, s0
	s_addc_u32 s1, s7, s1
	s_lshl_b32 s2, s2, 2
	s_add_u32 s0, s0, s2
	s_addc_u32 s1, s1, 0
	s_waitcnt vmcnt(42)
	ds_write_b128 v46, v[64:67]
	ds_write_b128 v47, v[68:71]
	s_waitcnt lgkmcnt(0)
	s_barrier
	ds_read_b64_tr_b16 v[48:49], v45
	ds_read_b64_tr_b16 v[50:51], v45 offset:576
	ds_read_b64_tr_b16 v[52:53], v45 offset:64
	ds_read_b64_tr_b16 v[54:55], v45 offset:640
	ds_read_b64_tr_b16 v[56:57], v45 offset:2304
	ds_read_b64_tr_b16 v[58:59], v45 offset:2880
	ds_read_b64_tr_b16 v[60:61], v45 offset:2368
	ds_read_b64_tr_b16 v[62:63], v45 offset:2944
	s_waitcnt vmcnt(41) lgkmcnt(4)
	v_mfma_f32_32x32x16_f16 v[2:17], v[128:131], v[48:51], 0
	v_mfma_f32_32x32x16_f16 v[18:33], v[128:131], v[52:55], 0
	ds_read_b64_tr_b16 v[48:49], v45 offset:4608
	ds_read_b64_tr_b16 v[50:51], v45 offset:5184
	ds_read_b64_tr_b16 v[52:53], v45 offset:4672
	ds_read_b64_tr_b16 v[54:55], v45 offset:5248
	s_waitcnt vmcnt(40) lgkmcnt(4)
	v_mfma_f32_32x32x16_f16 v[2:17], v[132:135], v[56:59], v[2:17]
	v_mfma_f32_32x32x16_f16 v[18:33], v[132:135], v[60:63], v[18:33]
	ds_read_b64_tr_b16 v[56:57], v45 offset:6912
	ds_read_b64_tr_b16 v[58:59], v45 offset:7488
	ds_read_b64_tr_b16 v[60:61], v45 offset:6976
	ds_read_b64_tr_b16 v[62:63], v45 offset:7552
	s_waitcnt vmcnt(39) lgkmcnt(4)
	v_mfma_f32_32x32x16_f16 v[2:17], v[136:139], v[48:51], v[2:17]
	v_mfma_f32_32x32x16_f16 v[18:33], v[136:139], v[52:55], v[18:33]
	s_waitcnt vmcnt(38) lgkmcnt(0)
	v_mfma_f32_32x32x16_f16 v[2:17], v[140:143], v[56:59], v[2:17]
	v_mfma_f32_32x32x16_f16 v[18:33], v[140:143], v[60:63], v[18:33]
	global_load_dwordx4 v[128:131], v[36:37], off
	global_load_dwordx4 v[132:135], v[36:37], off offset:1024
	global_load_dwordx4 v[136:139], v[36:37], off offset:2048
	global_load_dwordx4 v[140:143], v[36:37], off offset:3072
	s_waitcnt vmcnt(40)
	ds_write_b128 v46, v[72:75] offset:9216
	ds_write_b128 v47, v[76:79] offset:9216
	s_waitcnt lgkmcnt(0)
	s_barrier
	ds_read_b64_tr_b16 v[48:49], v45 offset:9216
	ds_read_b64_tr_b16 v[50:51], v45 offset:9792
	ds_read_b64_tr_b16 v[52:53], v45 offset:9280
	ds_read_b64_tr_b16 v[54:55], v45 offset:9856
	ds_read_b64_tr_b16 v[56:57], v45 offset:11520
	ds_read_b64_tr_b16 v[58:59], v45 offset:12096
	ds_read_b64_tr_b16 v[60:61], v45 offset:11584
	ds_read_b64_tr_b16 v[62:63], v45 offset:12160
	s_waitcnt vmcnt(39) lgkmcnt(4)
	v_mfma_f32_32x32x16_f16 v[2:17], v[144:147], v[48:51], v[2:17]
	v_mfma_f32_32x32x16_f16 v[18:33], v[144:147], v[52:55], v[18:33]
	ds_read_b64_tr_b16 v[48:49], v45 offset:13824
	ds_read_b64_tr_b16 v[50:51], v45 offset:14400
	ds_read_b64_tr_b16 v[52:53], v45 offset:13888
	ds_read_b64_tr_b16 v[54:55], v45 offset:14464
	s_waitcnt vmcnt(38) lgkmcnt(4)
	v_mfma_f32_32x32x16_f16 v[2:17], v[148:151], v[56:59], v[2:17]
	v_mfma_f32_32x32x16_f16 v[18:33], v[148:151], v[60:63], v[18:33]
	ds_read_b64_tr_b16 v[56:57], v45 offset:16128
	ds_read_b64_tr_b16 v[58:59], v45 offset:16704
	ds_read_b64_tr_b16 v[60:61], v45 offset:16192
	ds_read_b64_tr_b16 v[62:63], v45 offset:16768
	s_waitcnt vmcnt(37) lgkmcnt(4)
	v_mfma_f32_32x32x16_f16 v[2:17], v[152:155], v[48:51], v[2:17]
	v_mfma_f32_32x32x16_f16 v[18:33], v[152:155], v[52:55], v[18:33]
	s_waitcnt vmcnt(36) lgkmcnt(0)
	v_mfma_f32_32x32x16_f16 v[2:17], v[156:159], v[56:59], v[2:17]
	v_mfma_f32_32x32x16_f16 v[18:33], v[156:159], v[60:63], v[18:33]
	s_waitcnt vmcnt(34)
	ds_write_b128 v46, v[80:83]
	ds_write_b128 v47, v[84:87]
	s_waitcnt lgkmcnt(0)
	s_barrier
	ds_read_b64_tr_b16 v[48:49], v45
	ds_read_b64_tr_b16 v[50:51], v45 offset:576
	ds_read_b64_tr_b16 v[52:53], v45 offset:64
	ds_read_b64_tr_b16 v[54:55], v45 offset:640
	ds_read_b64_tr_b16 v[56:57], v45 offset:2304
	ds_read_b64_tr_b16 v[58:59], v45 offset:2880
	ds_read_b64_tr_b16 v[60:61], v45 offset:2368
	ds_read_b64_tr_b16 v[62:63], v45 offset:2944
	s_waitcnt vmcnt(33) lgkmcnt(4)
	v_mfma_f32_32x32x16_f16 v[2:17], v[160:163], v[48:51], v[2:17]
	v_mfma_f32_32x32x16_f16 v[18:33], v[160:163], v[52:55], v[18:33]
	ds_read_b64_tr_b16 v[48:49], v45 offset:4608
	ds_read_b64_tr_b16 v[50:51], v45 offset:5184
	ds_read_b64_tr_b16 v[52:53], v45 offset:4672
	ds_read_b64_tr_b16 v[54:55], v45 offset:5248
	s_waitcnt vmcnt(32) lgkmcnt(4)
	v_mfma_f32_32x32x16_f16 v[2:17], v[164:167], v[56:59], v[2:17]
	v_mfma_f32_32x32x16_f16 v[18:33], v[164:167], v[60:63], v[18:33]
	ds_read_b64_tr_b16 v[56:57], v45 offset:6912
	ds_read_b64_tr_b16 v[58:59], v45 offset:7488
	ds_read_b64_tr_b16 v[60:61], v45 offset:6976
	ds_read_b64_tr_b16 v[62:63], v45 offset:7552
	s_waitcnt vmcnt(31) lgkmcnt(4)
	v_mfma_f32_32x32x16_f16 v[2:17], v[168:171], v[48:51], v[2:17]
	v_mfma_f32_32x32x16_f16 v[18:33], v[168:171], v[52:55], v[18:33]
	s_waitcnt vmcnt(30) lgkmcnt(0)
	v_mfma_f32_32x32x16_f16 v[2:17], v[172:175], v[56:59], v[2:17]
	v_mfma_f32_32x32x16_f16 v[18:33], v[172:175], v[60:63], v[18:33]
	s_waitcnt vmcnt(28)
	ds_write_b128 v46, v[88:91] offset:9216
	ds_write_b128 v47, v[92:95] offset:9216
	s_waitcnt lgkmcnt(0)
	s_barrier
	ds_read_b64_tr_b16 v[48:49], v45 offset:9216
	ds_read_b64_tr_b16 v[50:51], v45 offset:9792
	ds_read_b64_tr_b16 v[52:53], v45 offset:9280
	ds_read_b64_tr_b16 v[54:55], v45 offset:9856
	ds_read_b64_tr_b16 v[56:57], v45 offset:11520
	ds_read_b64_tr_b16 v[58:59], v45 offset:12096
	ds_read_b64_tr_b16 v[60:61], v45 offset:11584
	ds_read_b64_tr_b16 v[62:63], v45 offset:12160
	s_waitcnt vmcnt(27) lgkmcnt(4)
	v_mfma_f32_32x32x16_f16 v[2:17], v[176:179], v[48:51], v[2:17]
	v_mfma_f32_32x32x16_f16 v[18:33], v[176:179], v[52:55], v[18:33]
	ds_read_b64_tr_b16 v[48:49], v45 offset:13824
	ds_read_b64_tr_b16 v[50:51], v45 offset:14400
	ds_read_b64_tr_b16 v[52:53], v45 offset:13888
	ds_read_b64_tr_b16 v[54:55], v45 offset:14464
	s_waitcnt vmcnt(26) lgkmcnt(4)
	v_mfma_f32_32x32x16_f16 v[2:17], v[180:183], v[56:59], v[2:17]
	v_mfma_f32_32x32x16_f16 v[18:33], v[180:183], v[60:63], v[18:33]
	ds_read_b64_tr_b16 v[56:57], v45 offset:16128
	ds_read_b64_tr_b16 v[58:59], v45 offset:16704
	ds_read_b64_tr_b16 v[60:61], v45 offset:16192
	ds_read_b64_tr_b16 v[62:63], v45 offset:16768
	s_waitcnt vmcnt(25) lgkmcnt(4)
	v_mfma_f32_32x32x16_f16 v[2:17], v[184:187], v[48:51], v[2:17]
	v_mfma_f32_32x32x16_f16 v[18:33], v[184:187], v[52:55], v[18:33]
	s_waitcnt vmcnt(24) lgkmcnt(0)
	v_mfma_f32_32x32x16_f16 v[2:17], v[188:191], v[56:59], v[2:17]
	v_mfma_f32_32x32x16_f16 v[18:33], v[188:191], v[60:63], v[18:33]
	s_waitcnt vmcnt(22)
	ds_write_b128 v46, v[96:99]
	ds_write_b128 v47, v[100:103]
	s_waitcnt lgkmcnt(0)
	s_barrier
	ds_read_b64_tr_b16 v[48:49], v45
	ds_read_b64_tr_b16 v[50:51], v45 offset:576
	ds_read_b64_tr_b16 v[52:53], v45 offset:64
	ds_read_b64_tr_b16 v[54:55], v45 offset:640
	ds_read_b64_tr_b16 v[56:57], v45 offset:2304
	ds_read_b64_tr_b16 v[58:59], v45 offset:2880
	ds_read_b64_tr_b16 v[60:61], v45 offset:2368
	ds_read_b64_tr_b16 v[62:63], v45 offset:2944
	s_waitcnt vmcnt(21) lgkmcnt(4)
	v_mfma_f32_32x32x16_f16 v[2:17], v[192:195], v[48:51], v[2:17]
	v_mfma_f32_32x32x16_f16 v[18:33], v[192:195], v[52:55], v[18:33]
	ds_read_b64_tr_b16 v[48:49], v45 offset:4608
	ds_read_b64_tr_b16 v[50:51], v45 offset:5184
	ds_read_b64_tr_b16 v[52:53], v45 offset:4672
	ds_read_b64_tr_b16 v[54:55], v45 offset:5248
	s_waitcnt vmcnt(20) lgkmcnt(4)
	v_mfma_f32_32x32x16_f16 v[2:17], v[196:199], v[56:59], v[2:17]
	v_mfma_f32_32x32x16_f16 v[18:33], v[196:199], v[60:63], v[18:33]
	ds_read_b64_tr_b16 v[56:57], v45 offset:6912
	ds_read_b64_tr_b16 v[58:59], v45 offset:7488
	ds_read_b64_tr_b16 v[60:61], v45 offset:6976
	ds_read_b64_tr_b16 v[62:63], v45 offset:7552
	s_waitcnt vmcnt(19) lgkmcnt(4)
	v_mfma_f32_32x32x16_f16 v[2:17], v[200:203], v[48:51], v[2:17]
	v_mfma_f32_32x32x16_f16 v[18:33], v[200:203], v[52:55], v[18:33]
	s_waitcnt vmcnt(18) lgkmcnt(0)
	v_mfma_f32_32x32x16_f16 v[2:17], v[204:207], v[56:59], v[2:17]
	v_mfma_f32_32x32x16_f16 v[18:33], v[204:207], v[60:63], v[18:33]
	s_waitcnt vmcnt(16)
	ds_write_b128 v46, v[104:107] offset:9216
	ds_write_b128 v47, v[108:111] offset:9216
	s_waitcnt lgkmcnt(0)
	s_barrier
	ds_read_b64_tr_b16 v[48:49], v45 offset:9216
	ds_read_b64_tr_b16 v[50:51], v45 offset:9792
	ds_read_b64_tr_b16 v[52:53], v45 offset:9280
	ds_read_b64_tr_b16 v[54:55], v45 offset:9856
	ds_read_b64_tr_b16 v[56:57], v45 offset:11520
	ds_read_b64_tr_b16 v[58:59], v45 offset:12096
	ds_read_b64_tr_b16 v[60:61], v45 offset:11584
	ds_read_b64_tr_b16 v[62:63], v45 offset:12160
	s_waitcnt vmcnt(15) lgkmcnt(4)
	v_mfma_f32_32x32x16_f16 v[2:17], v[208:211], v[48:51], v[2:17]
	v_mfma_f32_32x32x16_f16 v[18:33], v[208:211], v[52:55], v[18:33]
	ds_read_b64_tr_b16 v[48:49], v45 offset:13824
	ds_read_b64_tr_b16 v[50:51], v45 offset:14400
	ds_read_b64_tr_b16 v[52:53], v45 offset:13888
	ds_read_b64_tr_b16 v[54:55], v45 offset:14464
	s_waitcnt vmcnt(14) lgkmcnt(4)
	v_mfma_f32_32x32x16_f16 v[2:17], v[212:215], v[56:59], v[2:17]
	v_mfma_f32_32x32x16_f16 v[18:33], v[212:215], v[60:63], v[18:33]
	ds_read_b64_tr_b16 v[56:57], v45 offset:16128
	ds_read_b64_tr_b16 v[58:59], v45 offset:16704
	ds_read_b64_tr_b16 v[60:61], v45 offset:16192
	ds_read_b64_tr_b16 v[62:63], v45 offset:16768
	s_waitcnt vmcnt(13) lgkmcnt(4)
	v_mfma_f32_32x32x16_f16 v[2:17], v[216:219], v[48:51], v[2:17]
	v_mfma_f32_32x32x16_f16 v[18:33], v[216:219], v[52:55], v[18:33]
	s_waitcnt vmcnt(12) lgkmcnt(0)
	v_mfma_f32_32x32x16_f16 v[2:17], v[220:223], v[56:59], v[2:17]
	v_mfma_f32_32x32x16_f16 v[18:33], v[220:223], v[60:63], v[18:33]
	s_waitcnt vmcnt(10)
	ds_write_b128 v46, v[112:115]
	ds_write_b128 v47, v[116:119]
	s_waitcnt lgkmcnt(0)
	s_barrier
	ds_read_b64_tr_b16 v[48:49], v45
	ds_read_b64_tr_b16 v[50:51], v45 offset:576
	ds_read_b64_tr_b16 v[52:53], v45 offset:64
	ds_read_b64_tr_b16 v[54:55], v45 offset:640
	ds_read_b64_tr_b16 v[56:57], v45 offset:2304
	ds_read_b64_tr_b16 v[58:59], v45 offset:2880
	ds_read_b64_tr_b16 v[60:61], v45 offset:2368
	ds_read_b64_tr_b16 v[62:63], v45 offset:2944
	s_waitcnt vmcnt(9) lgkmcnt(4)
	v_mfma_f32_32x32x16_f16 v[2:17], v[224:227], v[48:51], v[2:17]
	v_mfma_f32_32x32x16_f16 v[18:33], v[224:227], v[52:55], v[18:33]
	ds_read_b64_tr_b16 v[48:49], v45 offset:4608
	ds_read_b64_tr_b16 v[50:51], v45 offset:5184
	ds_read_b64_tr_b16 v[52:53], v45 offset:4672
	ds_read_b64_tr_b16 v[54:55], v45 offset:5248
	s_waitcnt vmcnt(8) lgkmcnt(4)
	v_mfma_f32_32x32x16_f16 v[2:17], v[228:231], v[56:59], v[2:17]
	v_mfma_f32_32x32x16_f16 v[18:33], v[228:231], v[60:63], v[18:33]
	ds_read_b64_tr_b16 v[56:57], v45 offset:6912
	ds_read_b64_tr_b16 v[58:59], v45 offset:7488
	ds_read_b64_tr_b16 v[60:61], v45 offset:6976
	ds_read_b64_tr_b16 v[62:63], v45 offset:7552
	s_waitcnt vmcnt(7) lgkmcnt(4)
	v_mfma_f32_32x32x16_f16 v[2:17], v[232:235], v[48:51], v[2:17]
	v_mfma_f32_32x32x16_f16 v[18:33], v[232:235], v[52:55], v[18:33]
	s_waitcnt vmcnt(6) lgkmcnt(0)
	v_mfma_f32_32x32x16_f16 v[2:17], v[236:239], v[56:59], v[2:17]
	v_mfma_f32_32x32x16_f16 v[18:33], v[236:239], v[60:63], v[18:33]
	s_waitcnt vmcnt(4)
	ds_write_b128 v46, v[120:123] offset:9216
	ds_write_b128 v47, v[124:127] offset:9216
	s_waitcnt lgkmcnt(0)
	s_barrier
	ds_read_b64_tr_b16 v[48:49], v45 offset:9216
	ds_read_b64_tr_b16 v[50:51], v45 offset:9792
	ds_read_b64_tr_b16 v[52:53], v45 offset:9280
	ds_read_b64_tr_b16 v[54:55], v45 offset:9856
	ds_read_b64_tr_b16 v[56:57], v45 offset:11520
	ds_read_b64_tr_b16 v[58:59], v45 offset:12096
	ds_read_b64_tr_b16 v[60:61], v45 offset:11584
	ds_read_b64_tr_b16 v[62:63], v45 offset:12160
	s_waitcnt vmcnt(3) lgkmcnt(4)
	v_mfma_f32_32x32x16_f16 v[2:17], v[128:131], v[48:51], v[2:17]
	v_mfma_f32_32x32x16_f16 v[18:33], v[128:131], v[52:55], v[18:33]
	ds_read_b64_tr_b16 v[48:49], v45 offset:13824
	ds_read_b64_tr_b16 v[50:51], v45 offset:14400
	ds_read_b64_tr_b16 v[52:53], v45 offset:13888
	ds_read_b64_tr_b16 v[54:55], v45 offset:14464
	s_waitcnt vmcnt(2) lgkmcnt(4)
	v_mfma_f32_32x32x16_f16 v[2:17], v[132:135], v[56:59], v[2:17]
	v_mfma_f32_32x32x16_f16 v[18:33], v[132:135], v[60:63], v[18:33]
	ds_read_b64_tr_b16 v[56:57], v45 offset:16128
	ds_read_b64_tr_b16 v[58:59], v45 offset:16704
	ds_read_b64_tr_b16 v[60:61], v45 offset:16192
	ds_read_b64_tr_b16 v[62:63], v45 offset:16768
	s_waitcnt vmcnt(1) lgkmcnt(4)
	v_mfma_f32_32x32x16_f16 v[2:17], v[136:139], v[48:51], v[2:17]
	v_mfma_f32_32x32x16_f16 v[18:33], v[136:139], v[52:55], v[18:33]
	s_waitcnt vmcnt(0) lgkmcnt(0)
	s_barrier
	v_and_b32_e32 v34, 4, v44
	v_lshl_or_b32 v34, v43, 5, v34
	v_mul_u32_u24_e32 v34, 0x110, v34
	v_and_b32_e32 v36, 31, v0
	v_lshl_add_u32 v34, v36, 2, v34
	v_mfma_f32_32x32x16_f16 v[2:17], v[140:143], v[56:59], v[2:17]
	v_mfma_f32_32x32x16_f16 v[18:33], v[140:143], v[60:63], v[18:33]
	s_nop 11
	ds_write2_b32 v34, v2, v18 offset1:32
	ds_write2_b32 v34, v3, v19 offset0:68 offset1:100
	ds_write2_b32 v34, v4, v20 offset0:136 offset1:168
	ds_write2_b32 v34, v5, v21 offset0:204 offset1:236
	v_add_u32_e32 v2, 0x800, v34
	ds_write2_b32 v2, v6, v22 offset0:32 offset1:64
	ds_write2_b32 v2, v7, v23 offset0:100 offset1:132
	ds_write2_b32 v2, v8, v24 offset0:168 offset1:200
	v_add_u32_e32 v2, 0xa00, v34
	ds_write2_b32 v2, v9, v25 offset0:108 offset1:140
	v_add_u32_e32 v2, 0x1000, v34
	ds_write2_b32 v2, v10, v26 offset0:64 offset1:96
	ds_write2_b32 v2, v11, v27 offset0:132 offset1:164
	ds_write2_b32 v2, v12, v28 offset0:200 offset1:232
	v_add_u32_e32 v2, 0x1400, v34
	ds_write2_b32 v2, v13, v29 offset0:12 offset1:44
	v_add_u32_e32 v2, 0x1800, v34
	v_lshrrev_b32_e32 v4, 4, v0
	ds_write2_b32 v2, v14, v30 offset0:96 offset1:128
	ds_write2_b32 v2, v15, v31 offset0:164 offset1:196
	v_add_u32_e32 v2, 0x1a00, v34
	v_or_b32_e32 v10, s3, v4
	ds_write2_b32 v2, v16, v32 offset0:104 offset1:136
	v_add_u32_e32 v2, 0x1c00, v34
	v_ashrrev_i32_e32 v11, 31, v10
	ds_write2_b32 v2, v17, v33 offset0:44 offset1:76
	v_lshl_add_u64 v[2:3], v[10:11], 2, s[4:5]
	s_waitcnt lgkmcnt(0)
	s_barrier
	v_and_b32_e32 v34, 0xf0, v42
	s_movk_i32 s8, 0x110
	v_mad_u32_u24 v6, v4, s8, v34
	ds_read_b128 v[60:63], v6
	ds_read_b128 v[64:67], v6 offset:4352
	ds_read_b128 v[68:71], v6 offset:8704
	ds_read_b128 v[72:75], v6 offset:13056
	ds_read_b128 v[76:79], v6 offset:17408
	ds_read_b128 v[80:83], v6 offset:21760
	ds_read_b128 v[84:87], v6 offset:26112
	ds_read_b128 v[88:91], v6 offset:30464
	v_mov_b32_e32 v11, 0
	v_lshl_add_u64 v[14:15], s[0:1], 0, v[34:35]
	v_lshlrev_b64 v[12:13], 14, v[10:11]
	v_lshl_add_u64 v[12:13], v[14:15], 0, v[12:13]
	s_mov_b32 s10, 0x40000
	s_mov_b32 s11, 0
	s_waitcnt vmcnt(0)
	s_waitcnt lgkmcnt(7)
	v_pk_add_f32 v[60:61], v[60:61], v[240:241] op_sel_hi:[1,0]
	v_pk_add_f32 v[62:63], v[62:63], v[240:241] op_sel_hi:[1,0]
	global_store_dwordx4 v[12:13], v[60:63], off nt
	v_lshl_add_u64 v[12:13], v[12:13], 0, s[10:11]
	s_waitcnt lgkmcnt(6)
	v_pk_add_f32 v[64:65], v[64:65], v[242:243] op_sel_hi:[1,0]
	v_pk_add_f32 v[66:67], v[66:67], v[242:243] op_sel_hi:[1,0]
	global_store_dwordx4 v[12:13], v[64:67], off nt
	v_lshl_add_u64 v[12:13], v[12:13], 0, s[10:11]
	s_waitcnt lgkmcnt(5)
	v_pk_add_f32 v[68:69], v[68:69], v[244:245] op_sel_hi:[1,0]
	v_pk_add_f32 v[70:71], v[70:71], v[244:245] op_sel_hi:[1,0]
	global_store_dwordx4 v[12:13], v[68:71], off nt
	v_lshl_add_u64 v[12:13], v[12:13], 0, s[10:11]
	s_waitcnt lgkmcnt(4)
	v_pk_add_f32 v[72:73], v[72:73], v[246:247] op_sel_hi:[1,0]
	v_pk_add_f32 v[74:75], v[74:75], v[246:247] op_sel_hi:[1,0]
	global_store_dwordx4 v[12:13], v[72:75], off nt
	v_lshl_add_u64 v[12:13], v[12:13], 0, s[10:11]
	s_waitcnt lgkmcnt(3)
	v_pk_add_f32 v[76:77], v[76:77], v[248:249] op_sel_hi:[1,0]
	v_pk_add_f32 v[78:79], v[78:79], v[248:249] op_sel_hi:[1,0]
	global_store_dwordx4 v[12:13], v[76:79], off nt
	v_lshl_add_u64 v[12:13], v[12:13], 0, s[10:11]
	s_waitcnt lgkmcnt(2)
	v_pk_add_f32 v[80:81], v[80:81], v[250:251] op_sel_hi:[1,0]
	v_pk_add_f32 v[82:83], v[82:83], v[250:251] op_sel_hi:[1,0]
	global_store_dwordx4 v[12:13], v[80:83], off nt
	v_lshl_add_u64 v[12:13], v[12:13], 0, s[10:11]
	s_waitcnt lgkmcnt(1)
	v_pk_add_f32 v[84:85], v[84:85], v[252:253] op_sel_hi:[1,0]
	v_pk_add_f32 v[86:87], v[86:87], v[252:253] op_sel_hi:[1,0]
	global_store_dwordx4 v[12:13], v[84:87], off nt
	v_lshl_add_u64 v[12:13], v[12:13], 0, s[10:11]
	s_waitcnt lgkmcnt(0)
	v_pk_add_f32 v[88:89], v[88:89], v[254:255] op_sel_hi:[1,0]
	v_pk_add_f32 v[90:91], v[90:91], v[254:255] op_sel_hi:[1,0]
	global_store_dwordx4 v[12:13], v[88:91], off nt
	s_endpgm
	.p2alignl 8, 3212836864

	.amdhsa_kernel _Z9k_gemm_tlILi3ELb0EEvPKDF16_6TlArgs
		.amdhsa_group_segment_fixed_size 34816
		.amdhsa_private_segment_fixed_size 0
		.amdhsa_kernarg_size 80
		.amdhsa_user_sgpr_count 2
		.amdhsa_user_sgpr_dispatch_ptr 0
		.amdhsa_user_sgpr_queue_ptr 0
		.amdhsa_user_sgpr_kernarg_segment_ptr 1
		.amdhsa_user_sgpr_dispatch_id 0
		.amdhsa_user_sgpr_kernarg_preload_length 0
		.amdhsa_user_sgpr_kernarg_preload_offset 0
		.amdhsa_user_sgpr_private_segment_size 0
		.amdhsa_uses_dynamic_stack 0
		.amdhsa_enable_private_segment 0
		.amdhsa_system_sgpr_workgroup_id_x 1
		.amdhsa_system_sgpr_workgroup_id_y 1
		.amdhsa_system_sgpr_workgroup_id_z 0
		.amdhsa_system_sgpr_workgroup_info 0
		.amdhsa_system_vgpr_workitem_id 0
		.amdhsa_next_free_vgpr 256
		.amdhsa_next_free_sgpr 96
		.amdhsa_accum_offset 256
		.amdhsa_reserve_vcc 1
		.amdhsa_float_round_mode_32 0
		.amdhsa_float_round_mode_16_64 0
		.amdhsa_float_denorm_mode_32 3
		.amdhsa_float_denorm_mode_16_64 3
		.amdhsa_dx10_clamp 1
		.amdhsa_ieee_mode 1
		.amdhsa_fp16_overflow 0
		.amdhsa_tg_split 0
		.amdhsa_exception_fp_ieee_invalid_op 0
		.amdhsa_exception_fp_denorm_src 0
		.amdhsa_exception_fp_ieee_div_zero 0
		.amdhsa_exception_fp_ieee_overflow 0
		.amdhsa_exception_fp_ieee_underflow 0
		.amdhsa_exception_fp_ieee_inexact 0
		.amdhsa_exception_int_div_zero 0
	.end_amdhsa_kernel

amdhsa.kernels:
  - .agpr_count:     0
    .args:
      - .actual_access:  read_only
        .address_space:  global
        .offset:         0
        .size:           8
        .value_kind:     global_buffer
      - .actual_access:  read_only
        .address_space:  global
        .offset:         8
        .size:           8
        .value_kind:     global_buffer
      - .actual_access:  read_only
        .address_space:  global
        .offset:         16
        .size:           8
        .value_kind:     global_buffer
      - .actual_access:  write_only
        .address_space:  global
        .offset:         24
        .size:           8
        .value_kind:     global_buffer
      - .actual_access:  write_only
        .address_space:  global
        .offset:         32
        .size:           8
        .value_kind:     global_buffer
      - .actual_access:  write_only
        .address_space:  global
        .offset:         40
        .size:           8
        .value_kind:     global_buffer
      - .offset:         48
        .size:           104
        .value_kind:     by_value
    .group_segment_fixed_size: 37248
    .kernarg_segment_align: 8
    .kernarg_segment_size: 152
    .language:       OpenCL C
    .language_version:
      - 2
      - 0
    .max_flat_workgroup_size: 512
    .name:           _Z4k_lnPKfS0_S0_PDF16_PfS2_7CvtArgs
    .private_segment_fixed_size: 0
    .sgpr_count:     40
    .sgpr_spill_count: 0
    .symbol:         _Z4k_lnPKfS0_S0_PDF16_PfS2_7CvtArgs.kd
    .uniform_work_group_size: 1
    .uses_dynamic_stack: false
    .vgpr_count:     118
    .vgpr_spill_count: 0
    .wavefront_size: 64
  - .agpr_count:     36
    .args:
      - .actual_access:  read_only
        .address_space:  global
        .offset:         0
        .size:           8
        .value_kind:     global_buffer
      - .actual_access:  read_only
        .address_space:  global
        .offset:         8
        .size:           8
        .value_kind:     global_buffer
      - .actual_access:  read_only
        .address_space:  global
        .offset:         16
        .size:           8
        .value_kind:     global_buffer
      - .actual_access:  read_only
        .address_space:  global
        .offset:         24
        .size:           8
        .value_kind:     global_buffer
      - .actual_access:  read_only
        .address_space:  global
        .offset:         32
        .size:           8
        .value_kind:     global_buffer
      - .actual_access:  read_only
        .address_space:  global
        .offset:         40
        .size:           8
        .value_kind:     global_buffer
      - .actual_access:  read_only
        .address_space:  global
        .offset:         48
        .size:           8
        .value_kind:     global_buffer
      - .actual_access:  read_only
        .address_space:  global
        .offset:         56
        .size:           8
        .value_kind:     global_buffer
      - .actual_access:  write_only
        .address_space:  global
        .offset:         64
        .size:           8
        .value_kind:     global_buffer
      - .actual_access:  write_only
        .address_space:  global
        .offset:         72
        .size:           8
        .value_kind:     global_buffer
      - .actual_access:  write_only
        .address_space:  global
        .offset:         80
        .size:           8
        .value_kind:     global_buffer
      - .actual_access:  write_only
        .address_space:  global
        .offset:         88
        .size:           8
        .value_kind:     global_buffer
      - .actual_access:  write_only
        .address_space:  global
        .offset:         96
        .size:           8
        .value_kind:     global_buffer
    .group_segment_fixed_size: 77312
    .kernarg_segment_align: 8
    .kernarg_segment_size: 104
    .language:       OpenCL C
    .language_version:
      - 2
      - 0
    .max_flat_workgroup_size: 256
    .name:           _Z7k_frontPKDF16_S0_PKfS2_S0_S2_S2_S2_PjPfS4_S4_S4_
    .private_segment_fixed_size: 0
    .sgpr_count:     25
    .sgpr_spill_count: 0
    .symbol:         _Z7k_frontPKDF16_S0_PKfS2_S0_S2_S2_S2_PjPfS4_S4_S4_.kd
    .uniform_work_group_size: 1
    .uses_dynamic_stack: false
    .vgpr_count:     204
    .vgpr_spill_count: 0
    .wavefront_size: 64
  - .agpr_count:     0
    .args:
      - .actual_access:  read_only
        .address_space:  global
        .offset:         0
        .size:           8
        .value_kind:     global_buffer
      - .address_space:  global
        .offset:         8
        .size:           8
        .value_kind:     global_buffer
      - .actual_access:  read_only
        .address_space:  global
        .offset:         16
        .size:           8
        .value_kind:     global_buffer
    .group_segment_fixed_size: 0
    .kernarg_segment_align: 8
    .kernarg_segment_size: 24
    .language:       OpenCL C
    .language_version:
      - 2
      - 0
    .max_flat_workgroup_size: 64
    .name:           _Z7k_scan2PKfPfS0_
    .private_segment_fixed_size: 0
    .sgpr_count:     48
    .sgpr_spill_count: 0
    .symbol:         _Z7k_scan2PKfPfS0_.kd
    .uniform_work_group_size: 1
    .uses_dynamic_stack: false
    .vgpr_count:     150
    .vgpr_spill_count: 0
    .wavefront_size: 64
  - .agpr_count:     0
    .args:
      - .actual_access:  read_only
        .address_space:  global
        .offset:         0
        .size:           8
        .value_kind:     global_buffer
      - .actual_access:  read_only
        .address_space:  global
        .offset:         8
        .size:           8
        .value_kind:     global_buffer
      - .actual_access:  read_only
        .address_space:  global
        .offset:         16
        .size:           8
        .value_kind:     global_buffer
      - .actual_access:  read_only
        .address_space:  global
        .offset:         24
        .size:           8
        .value_kind:     global_buffer
      - .actual_access:  read_only
        .address_space:  global
        .offset:         32
        .size:           8
        .value_kind:     global_buffer
      - .actual_access:  read_only
        .address_space:  global
        .offset:         40
        .size:           8
        .value_kind:     global_buffer
      - .actual_access:  read_only
        .address_space:  global
        .offset:         48
        .size:           8
        .value_kind:     global_buffer
      - .actual_access:  read_only
        .address_space:  global
        .offset:         56
        .size:           8
        .value_kind:     global_buffer
      - .actual_access:  read_only
        .address_space:  global
        .offset:         64
        .size:           8
        .value_kind:     global_buffer
      - .offset:         72
        .size:           72
        .value_kind:     by_value
    .group_segment_fixed_size: 60416
    .kernarg_segment_align: 8
    .kernarg_segment_size: 144
    .language:       OpenCL C
    .language_version:
      - 2
      - 0
    .max_flat_workgroup_size: 256
    .name:           _Z7k_scan3PKjPKfS2_S2_S2_S2_PKDF16_S4_S4_7EpiArgs
    .private_segment_fixed_size: 0
    .sgpr_count:     34
    .sgpr_spill_count: 0
    .symbol:         _Z7k_scan3PKjPKfS2_S2_S2_S2_PKDF16_S4_S4_7EpiArgs.kd
    .uniform_work_group_size: 1
    .uses_dynamic_stack: false
    .vgpr_count:     236
    .vgpr_spill_count: 0
    .wavefront_size: 64
  - .agpr_count:     0
    .args:
      - .actual_access:  read_only
        .address_space:  global
        .offset:         0
        .size:           8
        .value_kind:     global_buffer
      - .actual_access:  read_only
        .address_space:  global
        .offset:         8
        .size:           8
        .value_kind:     global_buffer
      - .actual_access:  read_only
        .address_space:  global
        .offset:         16
        .size:           8
        .value_kind:     global_buffer
      - .actual_access:  write_only
        .address_space:  global
        .offset:         24
        .size:           8
        .value_kind:     global_buffer
    .group_segment_fixed_size: 20160
    .kernarg_segment_align: 8
    .kernarg_segment_size: 32
    .language:       OpenCL C
    .language_version:
      - 2
      - 0
    .max_flat_workgroup_size: 256
    .name:           _Z8k_dwconvPKDF16_PKfS2_PDF16_
    .private_segment_fixed_size: 0
    .sgpr_count:     86
    .sgpr_spill_count: 0
    .symbol:         _Z8k_dwconvPKDF16_PKfS2_PDF16_.kd
    .uniform_work_group_size: 1
    .uses_dynamic_stack: false
    .vgpr_count:     65
    .vgpr_spill_count: 0
    .wavefront_size: 64
  - .agpr_count:     0
    .args:
      - .actual_access:  read_only
        .address_space:  global
        .offset:         0
        .size:           8
        .value_kind:     global_buffer
      - .offset:         8
        .size:           72
        .value_kind:     by_value
    .group_segment_fixed_size: 38912
    .kernarg_segment_align: 8
    .kernarg_segment_size: 80
    .language:       OpenCL C
    .language_version:
      - 2
      - 0
    .max_flat_workgroup_size: 256
    .name:           _Z9k_gemm_tlILi2ELb1EEvPKDF16_6TlArgs
    .private_segment_fixed_size: 0
    .sgpr_count:     27
    .sgpr_spill_count: 0
    .symbol:         _Z9k_gemm_tlILi2ELb1EEvPKDF16_6TlArgs.kd
    .uniform_work_group_size: 1
    .uses_dynamic_stack: false
    .vgpr_count:     141
    .vgpr_spill_count: 0
    .wavefront_size: 64
  - .agpr_count:     0
    .args:
      - .actual_access:  read_only
        .address_space:  global
        .offset:         0
        .size:           8
        .value_kind:     global_buffer
      - .offset:         8
        .size:           72
        .value_kind:     by_value
    .group_segment_fixed_size: 34816
    .kernarg_segment_align: 8
    .kernarg_segment_size: 80
    .language:       OpenCL C
    .language_version:
      - 2
      - 0
    .max_flat_workgroup_size: 256
    .name:           _Z9k_gemm_tlILi3ELb0EEvPKDF16_6TlArgs
    .private_segment_fixed_size: 0
    .sgpr_count:     18
    .sgpr_spill_count: 0
    .symbol:         _Z9k_gemm_tlILi3ELb0EEvPKDF16_6TlArgs.kd
    .uniform_work_group_size: 1
    .uses_dynamic_stack: false
    .vgpr_count:     256
    .vgpr_spill_count: 0
    .wavefront_size: 64
